# MLA attention: fragment reads of each MFMA block issued up front into free registers, MFMAs behind counted lgkmcnt waits
# baseline (speedup 1.0000x reference)
.LBB0_822:
	s_or_b64 exec, exec, s[4:5]
	global_load_dwordx4 v[100:103], v[136:137], off
	s_andn2_b64 vcc, exec, s[12:13]
	s_cbranch_vccnz .LBB0_824
	s_mul_i32 s4, s7, 0x5600
	v_add_u32_e32 v2, s4, v148
	v_add_u32_e32 v56, 0x3000, v2
	ds_read2_b64 v[168:171], v56 offset0:128 offset1:130
	v_add_u32_e32 v2, 0x4000, v2
	ds_read2_b64 v[172:175], v2 offset0:160 offset1:162
	ds_read2_b64 v[176:179], v56 offset0:132 offset1:134
	ds_read2_b64 v[180:183], v2 offset0:164 offset1:166
	ds_read2_b64 v[184:187], v56 offset0:136 offset1:138
	ds_read2_b64 v[188:191], v2 offset0:168 offset1:170
	ds_read2_b64 v[192:195], v56 offset0:140 offset1:142
	ds_read2_b64 v[196:199], v2 offset0:172 offset1:174
	s_waitcnt lgkmcnt(7)
	v_mfma_f32_32x32x16_bf16 v[20:35], v[168:171], v[48:51], v[20:35]
	s_waitcnt lgkmcnt(6)
	v_mfma_f32_32x32x16_bf16 v[4:19], v[172:175], v[48:51], v[4:19]
	s_waitcnt lgkmcnt(5)
	v_mfma_f32_32x32x16_bf16 v[20:35], v[176:179], v[44:47], v[20:35]
	s_waitcnt lgkmcnt(4)
	v_mfma_f32_32x32x16_bf16 v[4:19], v[180:183], v[44:47], v[4:19]
	s_waitcnt lgkmcnt(3)
	v_mfma_f32_32x32x16_bf16 v[20:35], v[184:187], v[40:43], v[20:35]
	s_waitcnt lgkmcnt(2)
	v_mfma_f32_32x32x16_bf16 v[4:19], v[188:191], v[40:43], v[4:19]
	s_waitcnt lgkmcnt(1)
	v_mfma_f32_32x32x16_bf16 v[20:35], v[192:195], v[36:39], v[20:35]
	s_waitcnt lgkmcnt(0)
	v_mfma_f32_32x32x16_bf16 v[4:19], v[196:199], v[36:39], v[4:19]
.LBB0_824:
	s_add_i32 s4, s23, s20
	s_sub_i32 s12, s4, 60
	s_cmp_lt_i32 s12, 0
	s_cselect_b64 s[42:43], -1, 0
	s_add_i32 s5, s36, s37
	s_add_i32 s4, s5, 0xfffff100
	s_cmp_le_i32 s4, s22
	s_cselect_b64 s[44:45], -1, 0
	s_or_b64 s[42:43], s[42:43], s[44:45]
	s_andn2_b64 vcc, exec, s[42:43]
	s_cbranch_vccnz .LBB0_831
	s_mul_i32 s4, s8, 0x5600
	s_add_i32 s4, s4, 0
	v_add3_u32 v2, s4, v147, v106
	ds_read_b128 v[168:171], v2 offset:6656
	ds_read_b128 v[172:175], v2
	ds_read_b128 v[176:179], v2 offset:32
	ds_read_b128 v[180:183], v2 offset:6688
	s_cmp_gt_i32 s12, -1
	s_cselect_b64 s[12:13], -1, 0
	s_addk_i32 s5, 0xf13f
	s_cmp_gt_i32 s5, s9
	s_cselect_b64 s[42:43], -1, 0
	s_and_b64 s[12:13], s[12:13], s[42:43]
	s_andn2_b64 vcc, exec, s[12:13]
	ds_read_b128 v[184:187], v2 offset:64
	ds_read_b128 v[188:191], v2 offset:6720
	ds_read_b128 v[192:195], v2 offset:96
	ds_read_b128 v[196:199], v2 offset:6752
	ds_read_b128 v[208:211], v2 offset:128
	ds_read_b128 v[212:215], v2 offset:6784
	ds_read_b128 v[216:219], v2 offset:160
	ds_read_b128 v[220:223], v2 offset:6816
	s_waitcnt lgkmcnt(10)
	v_mfma_f32_32x32x16_bf16 v[52:67], v[172:175], v[88:91], 0
	v_mfma_f32_32x32x16_bf16 v[36:51], v[168:171], v[88:91], 0
	s_waitcnt lgkmcnt(9)
	v_mfma_f32_32x32x16_bf16 v[52:67], v[176:179], v[84:87], v[52:67]
	s_waitcnt lgkmcnt(8)
	v_mfma_f32_32x32x16_bf16 v[36:51], v[180:183], v[84:87], v[36:51]
	s_waitcnt lgkmcnt(7)
	v_mfma_f32_32x32x16_bf16 v[52:67], v[184:187], v[80:83], v[52:67]
	s_waitcnt lgkmcnt(6)
	v_mfma_f32_32x32x16_bf16 v[36:51], v[188:191], v[80:83], v[36:51]
	s_waitcnt lgkmcnt(5)
	v_mfma_f32_32x32x16_bf16 v[52:67], v[192:195], v[76:79], v[52:67]
	s_waitcnt lgkmcnt(4)
	v_mfma_f32_32x32x16_bf16 v[36:51], v[196:199], v[76:79], v[36:51]
	s_waitcnt lgkmcnt(3)
	v_mfma_f32_32x32x16_bf16 v[52:67], v[208:211], v[72:75], v[52:67]
	s_waitcnt lgkmcnt(2)
	v_mfma_f32_32x32x16_bf16 v[36:51], v[212:215], v[72:75], v[36:51]
	s_waitcnt lgkmcnt(1)
	v_mfma_f32_32x32x16_bf16 v[52:67], v[216:219], v[68:71], v[52:67]
	s_waitcnt lgkmcnt(0)
	v_mfma_f32_32x32x16_bf16 v[36:51], v[220:223], v[68:71], v[36:51]
	s_cbranch_vccnz .LBB0_827
	v_add_u32_e32 v2, s37, v124
	v_add_u32_e32 v152, 32, v2
	v_cmp_le_i32_e32 vcc, v152, v134
	v_add_u32_e32 v152, 33, v2
	s_nop 6
	v_cndmask_b32_e32 v36, v201, v36, vcc
	v_cmp_lt_i32_e32 vcc, v2, v134
	s_nop 1
	v_cndmask_b32_e32 v53, v201, v53, vcc
	v_cmp_le_i32_e32 vcc, v2, v134
	s_nop 1
	v_cndmask_b32_e32 v52, v201, v52, vcc
	v_cmp_le_i32_e32 vcc, v152, v134
	v_add_u32_e32 v152, 2, v2
	s_nop 0
	v_cndmask_b32_e32 v37, v201, v37, vcc
	v_cmp_le_i32_e32 vcc, v152, v134
	v_add_u32_e32 v152, 34, v2
	s_nop 0
	v_cndmask_b32_e32 v54, v201, v54, vcc
	v_cmp_le_i32_e32 vcc, v152, v134
	v_add_u32_e32 v152, 3, v2
	s_nop 0
	v_cndmask_b32_e32 v38, v201, v38, vcc
	v_cmp_le_i32_e32 vcc, v152, v134
	v_add_u32_e32 v152, 35, v2
	s_nop 0
	v_cndmask_b32_e32 v55, v201, v55, vcc
	v_cmp_le_i32_e32 vcc, v152, v134
	v_add_u32_e32 v152, 8, v2
	s_nop 0
	v_cndmask_b32_e32 v39, v201, v39, vcc
	v_cmp_le_i32_e32 vcc, v152, v134
	v_add_u32_e32 v152, 40, v2
	s_nop 0
	v_cndmask_b32_e32 v56, v201, v56, vcc
	v_cmp_le_i32_e32 vcc, v152, v134
	v_add_u32_e32 v152, 9, v2
	s_nop 0
	v_cndmask_b32_e32 v40, v201, v40, vcc
	v_cmp_le_i32_e32 vcc, v152, v134
	v_add_u32_e32 v152, 41, v2
	s_nop 0
	v_cndmask_b32_e32 v57, v201, v57, vcc
	v_cmp_le_i32_e32 vcc, v152, v134
	v_add_u32_e32 v152, 10, v2
	s_nop 0
	v_cndmask_b32_e32 v41, v201, v41, vcc
	v_cmp_le_i32_e32 vcc, v152, v134
	v_add_u32_e32 v152, 42, v2
	s_nop 0
	v_cndmask_b32_e32 v58, v201, v58, vcc
	v_cmp_le_i32_e32 vcc, v152, v134
	v_add_u32_e32 v152, 11, v2
	s_nop 0
	v_cndmask_b32_e32 v42, v201, v42, vcc
	v_cmp_le_i32_e32 vcc, v152, v134
	v_add_u32_e32 v152, 43, v2
	s_nop 0
	v_cndmask_b32_e32 v59, v201, v59, vcc
	v_cmp_le_i32_e32 vcc, v152, v134
	v_add_u32_e32 v152, 16, v2
	s_nop 0
	v_cndmask_b32_e32 v43, v201, v43, vcc
	v_cmp_le_i32_e32 vcc, v152, v134
	v_add_u32_e32 v152, 48, v2
	s_nop 0
	v_cndmask_b32_e32 v60, v201, v60, vcc
	v_cmp_le_i32_e32 vcc, v152, v134
	v_add_u32_e32 v152, 17, v2
	s_nop 0
	v_cndmask_b32_e32 v44, v201, v44, vcc
	v_cmp_le_i32_e32 vcc, v152, v134
	v_add_u32_e32 v152, 49, v2
	s_nop 0
	v_cndmask_b32_e32 v61, v201, v61, vcc
	v_cmp_le_i32_e32 vcc, v152, v134
	v_add_u32_e32 v152, 18, v2
	s_nop 0
	v_cndmask_b32_e32 v45, v201, v45, vcc
	v_cmp_le_i32_e32 vcc, v152, v134
	v_add_u32_e32 v152, 50, v2
	s_nop 0
	v_cndmask_b32_e32 v62, v201, v62, vcc
	v_cmp_le_i32_e32 vcc, v152, v134
	v_add_u32_e32 v152, 19, v2
	s_nop 0
	v_cndmask_b32_e32 v46, v201, v46, vcc
	v_cmp_le_i32_e32 vcc, v152, v134
	v_add_u32_e32 v152, 51, v2
	s_nop 0
	v_cndmask_b32_e32 v63, v201, v63, vcc
	v_cmp_le_i32_e32 vcc, v152, v134
	v_add_u32_e32 v152, 24, v2
	s_nop 0
	v_cndmask_b32_e32 v47, v201, v47, vcc
	v_cmp_le_i32_e32 vcc, v152, v134
	v_add_u32_e32 v152, 56, v2
	s_nop 0
	v_cndmask_b32_e32 v64, v201, v64, vcc
	v_cmp_le_i32_e32 vcc, v152, v134
	v_add_u32_e32 v152, 25, v2
	s_nop 0
	v_cndmask_b32_e32 v48, v201, v48, vcc
	v_cmp_le_i32_e32 vcc, v152, v134
	v_add_u32_e32 v152, 57, v2
	s_nop 0
	v_cndmask_b32_e32 v65, v201, v65, vcc
	v_cmp_le_i32_e32 vcc, v152, v134
	v_add_u32_e32 v152, 26, v2
	s_nop 0
	v_cndmask_b32_e32 v49, v201, v49, vcc
	v_cmp_le_i32_e32 vcc, v152, v134
	v_add_u32_e32 v152, 58, v2
	s_nop 0
	v_cndmask_b32_e32 v66, v201, v66, vcc
	v_cmp_le_i32_e32 vcc, v152, v134
	v_add_u32_e32 v152, 27, v2
	v_add_u32_e32 v2, 59, v2
	v_cndmask_b32_e32 v50, v201, v50, vcc
	v_cmp_le_i32_e32 vcc, v152, v134
	s_nop 1
	v_cndmask_b32_e32 v67, v201, v67, vcc
	v_cmp_le_i32_e32 vcc, v2, v134
	s_nop 1
	v_cndmask_b32_e32 v51, v201, v51, vcc

.LBB0_829:
	v_mul_f32_e32 v151, 0x3e16c740, v2
	v_fma_f32 v36, v36, s3, -v151
	v_exp_f32_e32 v154, v36
	v_fma_f32 v36, v53, s3, -v151
	v_fma_f32 v52, v52, s3, -v151
	v_exp_f32_e32 v155, v36
	v_fma_f32 v36, v37, s3, -v151
	v_exp_f32_e32 v153, v52
	v_exp_f32_e32 v156, v36
	v_fma_f32 v36, v54, s3, -v151
	v_exp_f32_e32 v157, v36
	v_fma_f32 v36, v38, s3, -v151
	v_fma_f32 v38, v55, s3, -v151
	v_exp_f32_e32 v158, v36
	v_exp_f32_e32 v159, v38
	v_fma_f32 v38, v39, s3, -v151
	v_exp_f32_e32 v160, v38
	v_add_f32_e32 v52, v153, v154
	v_add_f32_e32 v36, 0, v52
	v_add_f32_e32 v37, v155, v156
	v_add_f32_e32 v36, v37, v36
	v_add_f32_e32 v37, v157, v158
	v_fma_f32 v38, v56, s3, -v151
	v_add_f32_e32 v36, v37, v36
	v_add_f32_e32 v37, v159, v160
	v_exp_f32_e32 v161, v38
	v_fma_f32 v38, v40, s3, -v151
	v_add_f32_e32 v40, v37, v36
	v_fma_f32 v36, v57, s3, -v151
	v_exp_f32_e32 v163, v36
	v_fma_f32 v36, v41, s3, -v151
	v_exp_f32_e32 v164, v36
	v_fma_f32 v36, v58, s3, -v151
	v_exp_f32_e32 v162, v38
	v_exp_f32_e32 v37, v36
	v_fma_f32 v36, v42, s3, -v151
	v_exp_f32_e32 v39, v36
	v_fma_f32 v36, v59, s3, -v151
	v_fma_f32 v38, v43, s3, -v151
	v_exp_f32_e32 v36, v36
	v_exp_f32_e32 v38, v38
	v_add_f32_e32 v52, v161, v162
	v_add_f32_e32 v40, v52, v40
	v_add_f32_e32 v41, v163, v164
	v_add_f32_e32 v42, v41, v40
	v_pk_add_f32 v[40:41], v[36:37], v[38:39]
	v_pk_mov_b32 v[36:37], v[36:37], v[36:37] op_sel:[1,0]
	v_add_f32_e32 v41, v41, v42
	v_fma_f32 v42, v60, s3, -v151
	v_exp_f32_e32 v43, v42
	v_fma_f32 v42, v44, s3, -v151
	v_exp_f32_e32 v53, v42
	v_fma_f32 v42, v61, s3, -v151
	v_fma_f32 v44, v45, s3, -v151
	v_exp_f32_e32 v42, v42
	v_exp_f32_e32 v52, v44
	v_add_f32_e32 v44, v40, v41
	v_pk_mov_b32 v[38:39], v[38:39], v[38:39] op_sel:[1,0]
	s_andn2_b64 vcc, exec, s[18:19]
	v_pk_add_f32 v[40:41], v[42:43], v[52:53]
	v_pk_mov_b32 v[56:57], v[52:53], v[52:53] op_sel:[1,0]
	v_add_f32_e32 v41, v41, v44
	v_fma_f32 v44, v62, s3, -v151
	v_exp_f32_e32 v45, v44
	v_fma_f32 v44, v46, s3, -v151
	v_exp_f32_e32 v55, v44
	v_fma_f32 v44, v63, s3, -v151
	v_fma_f32 v46, v47, s3, -v151
	v_exp_f32_e32 v44, v44
	v_exp_f32_e32 v54, v46
	v_add_f32_e32 v46, v40, v41
	v_pk_mov_b32 v[42:43], v[42:43], v[42:43] op_sel:[1,0]
	v_pk_mov_b32 v[58:59], v[44:45], v[44:45] op_sel:[1,0]
	v_pk_add_f32 v[40:41], v[44:45], v[54:55]
	v_pk_mov_b32 v[54:55], v[54:55], v[54:55] op_sel:[1,0]
	v_add_f32_e32 v41, v41, v46
	v_fma_f32 v46, v64, s3, -v151
	v_exp_f32_e32 v47, v46
	v_fma_f32 v46, v48, s3, -v151
	v_exp_f32_e32 v53, v46
	v_fma_f32 v46, v65, s3, -v151
	v_fma_f32 v48, v49, s3, -v151
	v_exp_f32_e32 v46, v46
	v_exp_f32_e32 v52, v48
	v_add_f32_e32 v44, v40, v41
	v_fma_f32 v48, v51, s3, -v151
	v_exp_f32_e32 v48, v48
	v_pk_add_f32 v[40:41], v[46:47], v[52:53]
	v_pk_mov_b32 v[60:61], v[52:53], v[52:53] op_sel:[1,0]
	v_add_f32_e32 v41, v41, v44
	v_fma_f32 v44, v66, s3, -v151
	v_exp_f32_e32 v45, v44
	v_fma_f32 v44, v50, s3, -v151
	v_exp_f32_e32 v49, v44
	v_fma_f32 v44, v67, s3, -v151
	v_exp_f32_e32 v44, v44
	v_add_f32_e32 v50, v40, v41
	v_pk_mov_b32 v[46:47], v[46:47], v[46:47] op_sel:[1,0]
	v_pk_mov_b32 v[64:65], v[48:49], v[48:49] op_sel:[1,0]
	v_pk_add_f32 v[40:41], v[44:45], v[48:49]
	v_pk_mov_b32 v[62:63], v[44:45], v[44:45] op_sel:[1,0]
	v_add_f32_e32 v41, v41, v50
	v_add_f32_e32 v52, v40, v41
	ds_bpermute_b32 v53, v152, v52
	v_cvt_pk_bf16_f32 v48, v153, v155
	v_cvt_pk_bf16_f32 v49, v157, v159
	v_cvt_pk_bf16_f32 v50, v161, v163
	v_cvt_pk_bf16_f32 v51, v36, v37
	v_cvt_pk_bf16_f32 v44, v42, v43
	v_cvt_pk_bf16_f32 v45, v58, v59
	v_cvt_pk_bf16_f32 v46, v46, v47
	v_cvt_pk_bf16_f32 v47, v62, v63
	v_cvt_pk_bf16_f32 v40, v154, v156
	v_cvt_pk_bf16_f32 v41, v158, v160
	v_cvt_pk_bf16_f32 v42, v162, v164
	v_cvt_pk_bf16_f32 v43, v38, v39
	v_cvt_pk_bf16_f32 v36, v56, v57
	v_cvt_pk_bf16_f32 v37, v54, v55
	v_cvt_pk_bf16_f32 v38, v60, v61
	v_cvt_pk_bf16_f32 v39, v64, v65
	s_mov_b64 s[12:13], -1
	s_cbranch_vccnz .LBB0_832
	v_add3_u32 v58, s4, v146, v125
	v_add_u32_e32 v59, 0x3000, v58
	ds_read2_b64 v[168:171], v59 offset0:128 offset1:130
	v_add_u32_e32 v58, 0x4000, v58
	s_mov_b64 s[12:13], 0
	ds_read2_b64 v[172:175], v58 offset0:160 offset1:162
	ds_read2_b64 v[176:179], v59 offset0:132 offset1:134
	ds_read2_b64 v[180:183], v58 offset0:164 offset1:166
	ds_read2_b64 v[184:187], v59 offset0:136 offset1:138
	ds_read2_b64 v[188:191], v58 offset0:168 offset1:170
	ds_read2_b64 v[192:195], v59 offset0:140 offset1:142
	ds_read2_b64 v[196:199], v58 offset0:172 offset1:174
	s_waitcnt lgkmcnt(7)
	v_mfma_f32_32x32x16_bf16 v[20:35], v[168:171], v[48:51], v[20:35]
	s_waitcnt lgkmcnt(6)
	v_mfma_f32_32x32x16_bf16 v[4:19], v[172:175], v[48:51], v[4:19]
	s_waitcnt lgkmcnt(5)
	v_mfma_f32_32x32x16_bf16 v[20:35], v[176:179], v[44:47], v[20:35]
	s_waitcnt lgkmcnt(4)
	v_mfma_f32_32x32x16_bf16 v[4:19], v[180:183], v[44:47], v[4:19]
	s_waitcnt lgkmcnt(3)
	v_mfma_f32_32x32x16_bf16 v[20:35], v[184:187], v[40:43], v[20:35]
	s_waitcnt lgkmcnt(2)
	v_mfma_f32_32x32x16_bf16 v[4:19], v[188:191], v[40:43], v[4:19]
	s_waitcnt lgkmcnt(1)
	v_mfma_f32_32x32x16_bf16 v[20:35], v[192:195], v[36:39], v[20:35]
	s_waitcnt lgkmcnt(0)
	v_mfma_f32_32x32x16_bf16 v[4:19], v[196:199], v[36:39], v[4:19]
	s_branch .LBB0_833

.LBB0_838:
	s_andn2_b64 vcc, exec, s[12:13]
	s_cbranch_vccnz .LBB0_840
	s_mul_i32 s4, s7, 0x5600
	v_add_u32_e32 v56, s4, v148
	v_add_u32_e32 v57, 0x3000, v56
	ds_read2_b64 v[168:171], v57 offset0:128 offset1:130
	v_add_u32_e32 v56, 0x4000, v56
	ds_read2_b64 v[172:175], v56 offset0:160 offset1:162
	ds_read2_b64 v[176:179], v57 offset0:132 offset1:134
	ds_read2_b64 v[180:183], v56 offset0:164 offset1:166
	ds_read2_b64 v[184:187], v57 offset0:136 offset1:138
	ds_read2_b64 v[188:191], v56 offset0:168 offset1:170
	ds_read2_b64 v[192:195], v57 offset0:140 offset1:142
	ds_read2_b64 v[196:199], v56 offset0:172 offset1:174
	s_waitcnt lgkmcnt(7)
	v_mfma_f32_32x32x16_bf16 v[20:35], v[168:171], v[48:51], v[20:35]
	s_waitcnt lgkmcnt(6)
	v_mfma_f32_32x32x16_bf16 v[4:19], v[172:175], v[48:51], v[4:19]
	s_waitcnt lgkmcnt(5)
	v_mfma_f32_32x32x16_bf16 v[20:35], v[176:179], v[44:47], v[20:35]
	s_waitcnt lgkmcnt(4)
	v_mfma_f32_32x32x16_bf16 v[4:19], v[180:183], v[44:47], v[4:19]
	s_waitcnt lgkmcnt(3)
	v_mfma_f32_32x32x16_bf16 v[20:35], v[184:187], v[40:43], v[20:35]
	s_waitcnt lgkmcnt(2)
	v_mfma_f32_32x32x16_bf16 v[4:19], v[188:191], v[40:43], v[4:19]
	s_waitcnt lgkmcnt(1)
	v_mfma_f32_32x32x16_bf16 v[20:35], v[192:195], v[36:39], v[20:35]
	s_waitcnt lgkmcnt(0)
	v_mfma_f32_32x32x16_bf16 v[4:19], v[196:199], v[36:39], v[4:19]
.LBB0_840:
	s_lshl_b32 s4, s21, 2
	s_sub_i32 s13, s20, s4
	s_cmp_lt_i32 s13, 0
	s_cselect_b64 s[4:5], -1, 0
	s_lshl_b32 s12, s13, 6
	s_cmp_le_i32 s12, s22
	s_cselect_b64 s[22:23], -1, 0
	s_or_b64 s[4:5], s[4:5], s[22:23]
	s_andn2_b64 vcc, exec, s[4:5]
	s_mov_b64 s[4:5], 0
	s_cbranch_vccnz .LBB0_849
	v_add3_u32 v92, s42, v147, v106
	ds_read_b128 v[168:171], v92
	s_cmp_gt_i32 s13, -1
	s_cselect_b64 s[4:5], -1, 0
	s_or_b32 s12, s12, 63
	s_cmp_gt_i32 s12, s9
	s_cselect_b64 s[12:13], -1, 0
	s_and_b64 s[4:5], s[4:5], s[12:13]
	s_andn2_b64 vcc, exec, s[4:5]
	ds_read_b128 v[172:175], v92 offset:6656
	ds_read_b128 v[176:179], v92 offset:32
	ds_read_b128 v[180:183], v92 offset:6688
	ds_read_b128 v[184:187], v92 offset:64
	ds_read_b128 v[188:191], v92 offset:6720
	ds_read_b128 v[192:195], v92 offset:96
	ds_read_b128 v[196:199], v92 offset:6752
	ds_read_b128 v[208:211], v92 offset:128
	ds_read_b128 v[212:215], v92 offset:6784
	ds_read_b128 v[216:219], v92 offset:160
	ds_read_b128 v[220:223], v92 offset:6816
	s_waitcnt lgkmcnt(11)
	v_mfma_f32_32x32x16_bf16 v[52:67], v[168:171], v[88:91], 0
	s_waitcnt lgkmcnt(10)
	v_mfma_f32_32x32x16_bf16 v[36:51], v[172:175], v[88:91], 0
	s_waitcnt lgkmcnt(9)
	v_mfma_f32_32x32x16_bf16 v[52:67], v[176:179], v[84:87], v[52:67]
	s_waitcnt lgkmcnt(8)
	v_mfma_f32_32x32x16_bf16 v[36:51], v[180:183], v[84:87], v[36:51]
	s_waitcnt lgkmcnt(7)
	v_mfma_f32_32x32x16_bf16 v[52:67], v[184:187], v[80:83], v[52:67]
	s_waitcnt lgkmcnt(6)
	v_mfma_f32_32x32x16_bf16 v[36:51], v[188:191], v[80:83], v[36:51]
	s_waitcnt lgkmcnt(5)
	v_mfma_f32_32x32x16_bf16 v[52:67], v[192:195], v[76:79], v[52:67]
	s_waitcnt lgkmcnt(4)
	v_mfma_f32_32x32x16_bf16 v[36:51], v[196:199], v[76:79], v[36:51]
	s_waitcnt lgkmcnt(3)
	v_mfma_f32_32x32x16_bf16 v[52:67], v[208:211], v[72:75], v[52:67]
	s_waitcnt lgkmcnt(2)
	v_mfma_f32_32x32x16_bf16 v[36:51], v[212:215], v[72:75], v[36:51]
	s_waitcnt lgkmcnt(1)
	v_mfma_f32_32x32x16_bf16 v[52:67], v[216:219], v[68:71], v[52:67]
	s_waitcnt lgkmcnt(0)
	v_mfma_f32_32x32x16_bf16 v[36:51], v[220:223], v[68:71], v[36:51]
	s_cbranch_vccnz .LBB0_843
	v_lshl_or_b32 v68, s20, 6, v124
	v_or_b32_e32 v69, 32, v68
	v_cmp_le_i32_e32 vcc, v69, v134
	v_or_b32_e32 v69, 33, v68
	s_nop 6
	v_cndmask_b32_e32 v36, v201, v36, vcc
	v_cmp_lt_i32_e32 vcc, v68, v134
	s_nop 1
	v_cndmask_b32_e32 v53, v201, v53, vcc
	v_cmp_le_i32_e32 vcc, v68, v134
	s_nop 1
	v_cndmask_b32_e32 v52, v201, v52, vcc
	v_cmp_le_i32_e32 vcc, v69, v134
	v_or_b32_e32 v69, 2, v68
	s_nop 0
	v_cndmask_b32_e32 v37, v201, v37, vcc
	v_cmp_le_i32_e32 vcc, v69, v134
	v_or_b32_e32 v69, 34, v68
	s_nop 0
	v_cndmask_b32_e32 v54, v201, v54, vcc
	v_cmp_le_i32_e32 vcc, v69, v134
	v_or_b32_e32 v69, 3, v68
	s_nop 0
	v_cndmask_b32_e32 v38, v201, v38, vcc
	v_cmp_le_i32_e32 vcc, v69, v134
	v_or_b32_e32 v69, 35, v68
	s_nop 0
	v_cndmask_b32_e32 v55, v201, v55, vcc
	v_cmp_le_i32_e32 vcc, v69, v134
	v_or_b32_e32 v69, 8, v68
	s_nop 0
	v_cndmask_b32_e32 v39, v201, v39, vcc
	v_cmp_le_i32_e32 vcc, v69, v134
	v_or_b32_e32 v69, 40, v68
	s_nop 0
	v_cndmask_b32_e32 v56, v201, v56, vcc
	v_cmp_le_i32_e32 vcc, v69, v134
	v_or_b32_e32 v69, 9, v68
	s_nop 0
	v_cndmask_b32_e32 v40, v201, v40, vcc
	v_cmp_le_i32_e32 vcc, v69, v134
	v_or_b32_e32 v69, 41, v68
	s_nop 0
	v_cndmask_b32_e32 v57, v201, v57, vcc
	v_cmp_le_i32_e32 vcc, v69, v134
	v_or_b32_e32 v69, 10, v68
	s_nop 0
	v_cndmask_b32_e32 v41, v201, v41, vcc
	v_cmp_le_i32_e32 vcc, v69, v134
	v_or_b32_e32 v69, 42, v68
	s_nop 0
	v_cndmask_b32_e32 v58, v201, v58, vcc
	v_cmp_le_i32_e32 vcc, v69, v134
	v_or_b32_e32 v69, 11, v68
	s_nop 0
	v_cndmask_b32_e32 v42, v201, v42, vcc
	v_cmp_le_i32_e32 vcc, v69, v134
	v_or_b32_e32 v69, 43, v68
	s_nop 0
	v_cndmask_b32_e32 v59, v201, v59, vcc
	v_cmp_le_i32_e32 vcc, v69, v134
	v_or_b32_e32 v69, 16, v68
	s_nop 0
	v_cndmask_b32_e32 v43, v201, v43, vcc
	v_cmp_le_i32_e32 vcc, v69, v134
	v_or_b32_e32 v69, 48, v68
	s_nop 0
	v_cndmask_b32_e32 v60, v201, v60, vcc
	v_cmp_le_i32_e32 vcc, v69, v134
	v_or_b32_e32 v69, 17, v68
	s_nop 0
	v_cndmask_b32_e32 v44, v201, v44, vcc
	v_cmp_le_i32_e32 vcc, v69, v134
	v_or_b32_e32 v69, 49, v68
	s_nop 0
	v_cndmask_b32_e32 v61, v201, v61, vcc
	v_cmp_le_i32_e32 vcc, v69, v134
	v_or_b32_e32 v69, 18, v68
	s_nop 0
	v_cndmask_b32_e32 v45, v201, v45, vcc
	v_cmp_le_i32_e32 vcc, v69, v134
	v_or_b32_e32 v69, 50, v68
	s_nop 0
	v_cndmask_b32_e32 v62, v201, v62, vcc
	v_cmp_le_i32_e32 vcc, v69, v134
	v_or_b32_e32 v69, 19, v68
	s_nop 0
	v_cndmask_b32_e32 v46, v201, v46, vcc
	v_cmp_le_i32_e32 vcc, v69, v134
	v_or_b32_e32 v69, 51, v68
	s_nop 0
	v_cndmask_b32_e32 v63, v201, v63, vcc
	v_cmp_le_i32_e32 vcc, v69, v134
	v_or_b32_e32 v69, 24, v68
	s_nop 0
	v_cndmask_b32_e32 v47, v201, v47, vcc
	v_cmp_le_i32_e32 vcc, v69, v134
	v_or_b32_e32 v69, 56, v68
	s_nop 0
	v_cndmask_b32_e32 v64, v201, v64, vcc
	v_cmp_le_i32_e32 vcc, v69, v134
	v_or_b32_e32 v69, 25, v68
	s_nop 0
	v_cndmask_b32_e32 v48, v201, v48, vcc
	v_cmp_le_i32_e32 vcc, v69, v134
	v_or_b32_e32 v69, 57, v68
	s_nop 0
	v_cndmask_b32_e32 v65, v201, v65, vcc
	v_cmp_le_i32_e32 vcc, v69, v134
	v_or_b32_e32 v69, 26, v68
	s_nop 0
	v_cndmask_b32_e32 v49, v201, v49, vcc
	v_cmp_le_i32_e32 vcc, v69, v134
	v_or_b32_e32 v69, 58, v68
	s_nop 0
	v_cndmask_b32_e32 v66, v201, v66, vcc
	v_cmp_le_i32_e32 vcc, v69, v134
	v_or_b32_e32 v69, 27, v68
	v_or_b32_e32 v68, 59, v68
	v_cndmask_b32_e32 v50, v201, v50, vcc
	v_cmp_le_i32_e32 vcc, v69, v134
	s_nop 1
	v_cndmask_b32_e32 v67, v201, v67, vcc
	v_cmp_le_i32_e32 vcc, v68, v134
	s_nop 1
	v_cndmask_b32_e32 v51, v201, v51, vcc

.LBB0_845:
	v_mul_f32_e32 v2, 0x3e16c740, v69
	v_fma_f32 v36, v36, s3, -v2
	v_exp_f32_e32 v70, v36
	v_fma_f32 v36, v53, s3, -v2
	v_fma_f32 v52, v52, s3, -v2
	v_exp_f32_e32 v71, v36
	v_fma_f32 v36, v37, s3, -v2
	v_exp_f32_e32 v69, v52
	v_exp_f32_e32 v72, v36
	v_fma_f32 v36, v54, s3, -v2
	v_exp_f32_e32 v73, v36
	v_fma_f32 v36, v38, s3, -v2
	v_fma_f32 v38, v55, s3, -v2
	v_exp_f32_e32 v74, v36
	v_exp_f32_e32 v75, v38
	v_fma_f32 v38, v39, s3, -v2
	v_exp_f32_e32 v76, v38
	v_add_f32_e32 v52, v69, v70
	v_add_f32_e32 v36, 0, v52
	v_add_f32_e32 v37, v71, v72
	v_add_f32_e32 v36, v37, v36
	v_add_f32_e32 v37, v73, v74
	v_fma_f32 v38, v56, s3, -v2
	v_add_f32_e32 v36, v37, v36
	v_add_f32_e32 v37, v75, v76
	v_exp_f32_e32 v77, v38
	v_fma_f32 v38, v40, s3, -v2
	v_add_f32_e32 v40, v37, v36
	v_fma_f32 v36, v57, s3, -v2
	v_exp_f32_e32 v79, v36
	v_fma_f32 v36, v41, s3, -v2
	v_exp_f32_e32 v80, v36
	v_fma_f32 v36, v58, s3, -v2
	v_exp_f32_e32 v78, v38
	v_exp_f32_e32 v37, v36
	v_fma_f32 v36, v42, s3, -v2
	v_exp_f32_e32 v39, v36
	v_fma_f32 v36, v59, s3, -v2
	v_fma_f32 v38, v43, s3, -v2
	v_exp_f32_e32 v36, v36
	v_exp_f32_e32 v38, v38
	v_add_f32_e32 v52, v77, v78
	v_add_f32_e32 v40, v52, v40
	v_add_f32_e32 v41, v79, v80
	v_add_f32_e32 v42, v41, v40
	v_pk_add_f32 v[40:41], v[36:37], v[38:39]
	v_pk_mov_b32 v[36:37], v[36:37], v[36:37] op_sel:[1,0]
	v_add_f32_e32 v41, v41, v42
	v_fma_f32 v42, v60, s3, -v2
	v_exp_f32_e32 v43, v42
	v_fma_f32 v42, v44, s3, -v2
	v_exp_f32_e32 v53, v42
	v_fma_f32 v42, v61, s3, -v2
	v_fma_f32 v44, v45, s3, -v2
	v_exp_f32_e32 v42, v42
	v_exp_f32_e32 v52, v44
	v_add_f32_e32 v44, v40, v41
	v_pk_mov_b32 v[38:39], v[38:39], v[38:39] op_sel:[1,0]
	s_andn2_b64 vcc, exec, s[18:19]
	v_pk_add_f32 v[40:41], v[42:43], v[52:53]
	v_pk_mov_b32 v[56:57], v[52:53], v[52:53] op_sel:[1,0]
	v_add_f32_e32 v41, v41, v44
	v_fma_f32 v44, v62, s3, -v2
	v_exp_f32_e32 v45, v44
	v_fma_f32 v44, v46, s3, -v2
	v_exp_f32_e32 v55, v44
	v_fma_f32 v44, v63, s3, -v2
	v_fma_f32 v46, v47, s3, -v2
	v_exp_f32_e32 v44, v44
	v_exp_f32_e32 v54, v46
	v_add_f32_e32 v46, v40, v41
	v_pk_mov_b32 v[42:43], v[42:43], v[42:43] op_sel:[1,0]
	v_pk_mov_b32 v[58:59], v[44:45], v[44:45] op_sel:[1,0]
	v_pk_add_f32 v[40:41], v[44:45], v[54:55]
	v_pk_mov_b32 v[54:55], v[54:55], v[54:55] op_sel:[1,0]
	v_add_f32_e32 v41, v41, v46
	v_fma_f32 v46, v64, s3, -v2
	v_exp_f32_e32 v47, v46
	v_fma_f32 v46, v48, s3, -v2
	v_exp_f32_e32 v53, v46
	v_fma_f32 v46, v65, s3, -v2
	v_fma_f32 v48, v49, s3, -v2
	v_exp_f32_e32 v46, v46
	v_exp_f32_e32 v52, v48
	v_add_f32_e32 v44, v40, v41
	s_mov_b64 s[4:5], -1
	v_pk_add_f32 v[40:41], v[46:47], v[52:53]
	s_nop 0
	v_add_f32_e32 v41, v41, v44
	v_fma_f32 v44, v66, s3, -v2
	v_exp_f32_e32 v45, v44
	v_fma_f32 v44, v50, s3, -v2
	v_exp_f32_e32 v49, v44
	v_fma_f32 v44, v67, s3, -v2
	v_fma_f32 v2, v51, s3, -v2
	v_exp_f32_e32 v44, v44
	v_exp_f32_e32 v48, v2
	v_add_f32_e32 v2, v40, v41
	v_pk_mov_b32 v[60:61], v[52:53], v[52:53] op_sel:[1,0]
	v_pk_mov_b32 v[46:47], v[46:47], v[46:47] op_sel:[1,0]
	v_pk_add_f32 v[40:41], v[44:45], v[48:49]
	v_pk_mov_b32 v[62:63], v[44:45], v[44:45] op_sel:[1,0]
	v_add_f32_e32 v2, v41, v2
	v_add_f32_e32 v2, v40, v2
	ds_bpermute_b32 v52, v68, v2
	v_pk_mov_b32 v[64:65], v[48:49], v[48:49] op_sel:[1,0]
	v_cvt_pk_bf16_f32 v48, v69, v71
	v_cvt_pk_bf16_f32 v49, v73, v75
	v_cvt_pk_bf16_f32 v50, v77, v79
	v_cvt_pk_bf16_f32 v51, v36, v37
	v_cvt_pk_bf16_f32 v44, v42, v43
	v_cvt_pk_bf16_f32 v45, v58, v59
	v_cvt_pk_bf16_f32 v46, v46, v47
	v_cvt_pk_bf16_f32 v47, v62, v63
	v_cvt_pk_bf16_f32 v40, v70, v72
	v_cvt_pk_bf16_f32 v41, v74, v76
	v_cvt_pk_bf16_f32 v42, v78, v80
	v_cvt_pk_bf16_f32 v43, v38, v39
	v_cvt_pk_bf16_f32 v36, v56, v57
	v_cvt_pk_bf16_f32 v37, v54, v55
	v_cvt_pk_bf16_f32 v38, v60, v61
	v_cvt_pk_bf16_f32 v39, v64, v65
	s_cbranch_vccnz .LBB0_847
	v_add3_u32 v53, s42, v146, v125
	v_add_u32_e32 v58, 0x3000, v53
	ds_read2_b64 v[168:171], v58 offset0:128 offset1:130
	v_add_u32_e32 v53, 0x4000, v53
	s_mov_b64 s[4:5], 0
	ds_read2_b64 v[172:175], v53 offset0:160 offset1:162
	ds_read2_b64 v[176:179], v58 offset0:132 offset1:134
	ds_read2_b64 v[180:183], v53 offset0:164 offset1:166
	ds_read2_b64 v[184:187], v58 offset0:136 offset1:138
	ds_read2_b64 v[188:191], v53 offset0:168 offset1:170
	ds_read2_b64 v[192:195], v58 offset0:140 offset1:142
	ds_read2_b64 v[196:199], v53 offset0:172 offset1:174
	s_waitcnt lgkmcnt(7)
	v_mfma_f32_32x32x16_bf16 v[20:35], v[168:171], v[48:51], v[20:35]
	s_waitcnt lgkmcnt(6)
	v_mfma_f32_32x32x16_bf16 v[4:19], v[172:175], v[48:51], v[4:19]
	s_waitcnt lgkmcnt(5)
	v_mfma_f32_32x32x16_bf16 v[20:35], v[176:179], v[44:47], v[20:35]
	s_waitcnt lgkmcnt(4)
	v_mfma_f32_32x32x16_bf16 v[4:19], v[180:183], v[44:47], v[4:19]
	s_waitcnt lgkmcnt(3)
	v_mfma_f32_32x32x16_bf16 v[20:35], v[184:187], v[40:43], v[20:35]
	s_waitcnt lgkmcnt(2)
	v_mfma_f32_32x32x16_bf16 v[4:19], v[188:191], v[40:43], v[4:19]
	s_waitcnt lgkmcnt(1)
	v_mfma_f32_32x32x16_bf16 v[20:35], v[192:195], v[36:39], v[20:35]
	s_waitcnt lgkmcnt(0)
	v_mfma_f32_32x32x16_bf16 v[4:19], v[196:199], v[36:39], v[4:19]
	s_branch .LBB0_848

.LBB0_849:
	s_and_b64 vcc, exec, s[4:5]
	s_barrier
	s_cbranch_vccz .LBB0_809
	s_mul_i32 s4, s7, 0x5600
	v_add_u32_e32 v2, s4, v148
	v_add_u32_e32 v56, 0x3000, v2
	ds_read2_b64 v[168:171], v56 offset0:128 offset1:130
	v_add_u32_e32 v2, 0x4000, v2
	ds_read2_b64 v[172:175], v2 offset0:160 offset1:162
	ds_read2_b64 v[176:179], v56 offset0:132 offset1:134
	ds_read2_b64 v[180:183], v2 offset0:164 offset1:166
	ds_read2_b64 v[184:187], v56 offset0:136 offset1:138
	ds_read2_b64 v[188:191], v2 offset0:168 offset1:170
	ds_read2_b64 v[192:195], v56 offset0:140 offset1:142
	ds_read2_b64 v[196:199], v2 offset0:172 offset1:174
	s_waitcnt lgkmcnt(7)
	v_mfma_f32_32x32x16_bf16 v[20:35], v[168:171], v[48:51], v[20:35]
	s_waitcnt lgkmcnt(6)
	v_mfma_f32_32x32x16_bf16 v[4:19], v[172:175], v[48:51], v[4:19]
	s_waitcnt lgkmcnt(5)
	v_mfma_f32_32x32x16_bf16 v[20:35], v[176:179], v[44:47], v[20:35]
	s_waitcnt lgkmcnt(4)
	v_mfma_f32_32x32x16_bf16 v[4:19], v[180:183], v[44:47], v[4:19]
	s_waitcnt lgkmcnt(3)
	v_mfma_f32_32x32x16_bf16 v[20:35], v[184:187], v[40:43], v[20:35]
	s_waitcnt lgkmcnt(2)
	v_mfma_f32_32x32x16_bf16 v[4:19], v[188:191], v[40:43], v[4:19]
	s_waitcnt lgkmcnt(1)
	v_mfma_f32_32x32x16_bf16 v[20:35], v[192:195], v[36:39], v[20:35]
	s_waitcnt lgkmcnt(0)
	v_mfma_f32_32x32x16_bf16 v[4:19], v[196:199], v[36:39], v[4:19]
	s_branch .LBB0_809
